# v8: + redundant SGPR tuple reloads (26 v_readlane per K-loop body) removed from the P1 side job
# speedup vs baseline: 1.0040x; 1.0040x over previous
; #define PG8_LAS __attribute__((address_space(3)))
;     __device__ __forceinline__ void issue(PG8_LAS unsigned char* lds0, int j, int tid, int wid) const {
;         const float* s0; unsigned char* d; addr(j, tid, s0, d);
;         __builtin_amdgcn_global_load_lds((const unsigned*)s0, (PG8_LAS unsigned*)(lds0 + stage + wid * 1024), 16, 0, 2);
;         __builtin_amdgcn_global_load_lds((const unsigned*)(s0 + ntot), (PG8_LAS unsigned*)(lds0 + stage + 8192 + wid * 1024), 16, 0, 2);
.LBB0_172:
	s_cmpk_lt_i32 s77, 0x60
	s_cselect_b64 s[2:3], -1, 0
	s_cmpk_gt_i32 s77, 0x5f
	s_cbranch_scc1 .LBB0_174
	s_add_i32 s56, s77, s68
	s_lshr_b32 s4, s56, 31
	s_add_i32 s4, s56, s4
	s_ashr_i32 s57, s4, 1
	s_ashr_i32 s4, s4, 11
	s_ashr_i32 s5, s4, 31
	v_readlane_b32 s8, v251, 32
	s_lshl_b64 s[4:5], s[4:5], 25
	v_readlane_b32 s12, v251, 36
	v_readlane_b32 s13, v251, 37
	s_add_u32 s4, s12, s4
	s_addc_u32 s5, s13, s5
	s_lshl_b32 s82, s57, 15
	s_and_b32 s82, s82, 0x1ff8000
	s_add_u32 s82, s4, s82
	s_addc_u32 s83, s5, 0
	s_lshl_b32 s4, s57, 12
	s_lshl_b32 s5, s56, 11
	s_sub_i32 s4, s5, s4
	s_ashr_i32 s5, s4, 31
	s_lshl_b64 s[4:5], s[4:5], 2
	s_add_u32 s4, s82, s4
	s_addc_u32 s5, s83, s5
	v_lshlrev_b32_e32 v2, 2, v208
	v_lshl_add_u64 v[4:5], s[4:5], 0, v[2:3]
	s_add_i32 m0, s41, 0x24000
	v_lshl_add_u64 v[4:5], v[4:5], 0, s[42:43]
	global_load_lds_dwordx4 v2, s[4:5] nt
	s_add_i32 m0, s41, 0x26000
	s_add_i32 s77, s77, 1
	global_load_lds_dwordx4 v[4:5], off nt
.LBB0_174:
	s_add_u32 s4, s54, 0xfff80080
	s_addc_u32 s5, s55, -1
	s_cmp_eq_u32 s81, 28
	s_cselect_b32 s5, s7, s5
	s_cselect_b32 s4, s33, s4
	s_cselect_b32 s57, s45, s80
	s_cselect_b32 s56, s47, s79
	s_barrier
	s_setprio 1
	s_waitcnt lgkmcnt(0)
	v_mfma_f32_16x16x32_bf16 v[138:141], v[158:161], v[198:201], v[138:141]
	v_mfma_f32_16x16x32_bf16 v[134:137], v[166:169], v[198:201], v[134:137]
	v_mfma_f32_16x16x32_bf16 v[122:125], v[158:161], v[190:193], v[122:125]
	v_mfma_f32_16x16x32_bf16 v[118:121], v[166:169], v[190:193], v[118:121]
	v_mfma_f32_16x16x32_bf16 v[106:109], v[158:161], v[182:185], v[106:109]
	v_mfma_f32_16x16x32_bf16 v[102:105], v[166:169], v[182:185], v[102:105]
	v_mfma_f32_16x16x32_bf16 v[90:93], v[158:161], v[174:177], v[90:93]
	v_mfma_f32_16x16x32_bf16 v[86:89], v[166:169], v[174:177], v[86:89]
	v_mfma_f32_16x16x32_bf16 v[138:141], v[162:165], v[202:205], v[138:141]
	v_mfma_f32_16x16x32_bf16 v[134:137], v[170:173], v[202:205], v[134:137]
	v_mfma_f32_16x16x32_bf16 v[122:125], v[162:165], v[194:197], v[122:125]
	v_mfma_f32_16x16x32_bf16 v[118:121], v[170:173], v[194:197], v[118:121]
	v_mfma_f32_16x16x32_bf16 v[106:109], v[162:165], v[186:189], v[106:109]
	v_mfma_f32_16x16x32_bf16 v[102:105], v[170:173], v[186:189], v[102:105]
	v_mfma_f32_16x16x32_bf16 v[90:93], v[162:165], v[178:181], v[90:93]
	v_mfma_f32_16x16x32_bf16 v[86:89], v[170:173], v[178:181], v[86:89]
	s_setprio 0
	s_setprio 1
	v_mfma_f32_16x16x32_bf16 v[130:133], v[142:145], v[198:201], v[130:133]
	v_mfma_f32_16x16x32_bf16 v[126:129], v[150:153], v[198:201], v[126:129]
	v_mfma_f32_16x16x32_bf16 v[114:117], v[142:145], v[190:193], v[114:117]
	v_mfma_f32_16x16x32_bf16 v[110:113], v[150:153], v[190:193], v[110:113]
	v_mfma_f32_16x16x32_bf16 v[98:101], v[142:145], v[182:185], v[98:101]
	v_mfma_f32_16x16x32_bf16 v[94:97], v[150:153], v[182:185], v[94:97]
	v_mfma_f32_16x16x32_bf16 v[82:85], v[142:145], v[174:177], v[82:85]
	v_mfma_f32_16x16x32_bf16 v[78:81], v[150:153], v[174:177], v[78:81]
	v_mfma_f32_16x16x32_bf16 v[130:133], v[146:149], v[202:205], v[130:133]
	v_mfma_f32_16x16x32_bf16 v[126:129], v[154:157], v[202:205], v[126:129]
	v_mfma_f32_16x16x32_bf16 v[114:117], v[146:149], v[194:197], v[114:117]
	v_mfma_f32_16x16x32_bf16 v[110:113], v[154:157], v[194:197], v[110:113]
	v_mfma_f32_16x16x32_bf16 v[98:101], v[146:149], v[186:189], v[98:101]
	v_mfma_f32_16x16x32_bf16 v[94:97], v[154:157], v[186:189], v[94:97]
	v_mfma_f32_16x16x32_bf16 v[82:85], v[146:149], v[178:181], v[82:85]
	v_mfma_f32_16x16x32_bf16 v[78:81], v[154:157], v[178:181], v[78:81]
	s_setprio 0
	s_barrier
	s_mov_b32 m0, s53
	v_lshl_add_u64 v[4:5], s[56:57], 0, v[212:213]
	s_add_u32 s82, s56, 0x80000
	ds_read_b128 v[174:177], v234 offset:16384
	ds_read_b128 v[178:181], v234 offset:17408
	ds_read_b128 v[182:185], v234 offset:18432
	ds_read_b128 v[186:189], v234 offset:19456
	ds_read_b128 v[190:193], v234 offset:20480
	ds_read_b128 v[194:197], v234 offset:21504
	ds_read_b128 v[198:201], v234 offset:22528
	ds_read_b128 v[202:205], v234 offset:23552
	global_load_lds_dwordx4 v[4:5], off
	v_lshl_add_u64 v[226:227], s[56:57], 0, v[216:217]
	s_mov_b32 m0, s60
	s_addc_u32 s83, s57, 0
	global_load_lds_dwordx4 v[226:227], off
	v_lshl_add_u64 v[228:229], s[82:83], 0, v[212:213]
	s_mov_b32 m0, s61
	v_lshl_add_u64 v[230:231], s[4:5], 0, v[214:215]
	global_load_lds_dwordx4 v[228:229], off
	v_lshl_add_u64 v[228:229], s[82:83], 0, v[216:217]
	s_mov_b32 m0, s64
	s_nop 0
	global_load_lds_dwordx4 v[228:229], off
	v_lshl_add_u64 v[228:229], s[4:5], 0, v[210:211]
	s_mov_b32 m0, s41
	s_nop 0
	global_load_lds_dwordx4 v[228:229], off
	s_mov_b32 m0, s65
	s_nop 0
	global_load_lds_dwordx4 v[230:231], off
	s_waitcnt vmcnt(8)
	s_waitcnt lgkmcnt(0)
	s_barrier
	s_setprio 1
	s_waitcnt lgkmcnt(0)
	v_mfma_f32_16x16x32_bf16 v[74:77], v[158:161], v[174:177], v[74:77]
	v_mfma_f32_16x16x32_bf16 v[70:73], v[166:169], v[174:177], v[70:73]
	v_mfma_f32_16x16x32_bf16 v[58:61], v[158:161], v[182:185], v[58:61]
	v_mfma_f32_16x16x32_bf16 v[54:57], v[166:169], v[182:185], v[54:57]
	v_mfma_f32_16x16x32_bf16 v[42:45], v[158:161], v[190:193], v[42:45]
	v_mfma_f32_16x16x32_bf16 v[38:41], v[166:169], v[190:193], v[38:41]
	v_mfma_f32_16x16x32_bf16 v[26:29], v[158:161], v[198:201], v[26:29]
	v_mfma_f32_16x16x32_bf16 v[22:25], v[166:169], v[198:201], v[22:25]
	v_mfma_f32_16x16x32_bf16 v[74:77], v[162:165], v[178:181], v[74:77]
	v_mfma_f32_16x16x32_bf16 v[70:73], v[170:173], v[178:181], v[70:73]
	v_mfma_f32_16x16x32_bf16 v[58:61], v[162:165], v[186:189], v[58:61]
	v_mfma_f32_16x16x32_bf16 v[54:57], v[170:173], v[186:189], v[54:57]
	v_mfma_f32_16x16x32_bf16 v[42:45], v[162:165], v[194:197], v[42:45]
	v_mfma_f32_16x16x32_bf16 v[38:41], v[170:173], v[194:197], v[38:41]
	v_mfma_f32_16x16x32_bf16 v[26:29], v[162:165], v[202:205], v[26:29]
	v_mfma_f32_16x16x32_bf16 v[22:25], v[170:173], v[202:205], v[22:25]
	s_setprio 0
	s_setprio 1
	v_mfma_f32_16x16x32_bf16 v[66:69], v[142:145], v[174:177], v[66:69]
	v_mfma_f32_16x16x32_bf16 v[62:65], v[150:153], v[174:177], v[62:65]
	v_mfma_f32_16x16x32_bf16 v[50:53], v[142:145], v[182:185], v[50:53]
	v_mfma_f32_16x16x32_bf16 v[46:49], v[150:153], v[182:185], v[46:49]
	v_mfma_f32_16x16x32_bf16 v[34:37], v[142:145], v[190:193], v[34:37]
	v_mfma_f32_16x16x32_bf16 v[30:33], v[150:153], v[190:193], v[30:33]
	v_mfma_f32_16x16x32_bf16 v[18:21], v[142:145], v[198:201], v[18:21]
	v_mfma_f32_16x16x32_bf16 v[14:17], v[150:153], v[198:201], v[14:17]
	v_mfma_f32_16x16x32_bf16 v[66:69], v[146:149], v[178:181], v[66:69]
	v_mfma_f32_16x16x32_bf16 v[62:65], v[154:157], v[178:181], v[62:65]
	v_mfma_f32_16x16x32_bf16 v[50:53], v[146:149], v[186:189], v[50:53]
	v_mfma_f32_16x16x32_bf16 v[46:49], v[154:157], v[186:189], v[46:49]
	v_mfma_f32_16x16x32_bf16 v[34:37], v[146:149], v[194:197], v[34:37]
	v_mfma_f32_16x16x32_bf16 v[30:33], v[154:157], v[194:197], v[30:33]
	v_mfma_f32_16x16x32_bf16 v[18:21], v[146:149], v[202:205], v[18:21]
	v_mfma_f32_16x16x32_bf16 v[14:17], v[154:157], v[202:205], v[14:17]
	s_setprio 0
	s_barrier
	v_add_u32_e32 v2, 0x18000, v209
	ds_read_b128 v[158:161], v2
	ds_read_b128 v[162:165], v2 offset:1024
	ds_read_b128 v[166:169], v2 offset:2048
	ds_read_b128 v[170:173], v2 offset:3072
	v_add_u32_e32 v2, 0x1c000, v209
	ds_read_b128 v[142:145], v2
	ds_read_b128 v[146:149], v2 offset:1024
	ds_read_b128 v[150:153], v2 offset:2048
	ds_read_b128 v[154:157], v2 offset:3072
	s_add_u32 s4, s4, 0x80000
	s_addc_u32 s5, s5, 0
	s_mov_b32 m0, s66
	v_lshl_add_u64 v[238:239], s[4:5], 0, v[210:211]
	ds_read_b128 v[198:201], v234 offset:32768
	ds_read_b128 v[202:205], v234 offset:33792
	ds_read_b128 v[190:193], v234 offset:34816
	ds_read_b128 v[194:197], v234 offset:35840
	ds_read_b128 v[182:185], v234 offset:36864
	ds_read_b128 v[186:189], v234 offset:37888
	ds_read_b128 v[174:177], v234 offset:38912
	ds_read_b128 v[178:181], v234 offset:39936
	global_load_lds_dwordx4 v[238:239], off
	v_lshl_add_u64 v[238:239], s[4:5], 0, v[214:215]
	s_mov_b32 m0, s67
	v_cndmask_b32_e64 v2, 0, 1, s[2:3]
	global_load_lds_dwordx4 v[238:239], off
	s_waitcnt vmcnt(8)
	v_cmp_ne_u32_e64 s[4:5], 1, v2
	s_andn2_b64 vcc, exec, s[2:3]
	s_cbranch_vccnz .LBB0_176
	ds_read_b128 v[6:9], v207
	ds_read_b128 v[10:13], v1

; #define PG8_LAS __attribute__((address_space(3)))
;     __device__ __forceinline__ void issue(PG8_LAS unsigned char* lds0, int j, int tid, int wid) const {
;         const float* s0; unsigned char* d; addr(j, tid, s0, d);
;         __builtin_amdgcn_global_load_lds((const unsigned*)s0, (PG8_LAS unsigned*)(lds0 + stage + wid * 1024), 16, 0, 2);
;         __builtin_amdgcn_global_load_lds((const unsigned*)(s0 + ntot), (PG8_LAS unsigned*)(lds0 + stage + 8192 + wid * 1024), 16, 0, 2);
.LBB0_178:
	s_cmpk_lt_i32 s77, 0x60
	s_cselect_b64 s[2:3], -1, 0
	s_cmpk_gt_i32 s77, 0x5f
	s_cbranch_scc1 .LBB0_167
	s_add_i32 s82, s77, s68
	s_lshr_b32 s4, s82, 31
	s_add_i32 s4, s82, s4
	s_ashr_i32 s83, s4, 1
	s_ashr_i32 s4, s4, 11
	s_ashr_i32 s5, s4, 31
	v_readlane_b32 s8, v251, 32
	s_lshl_b64 s[4:5], s[4:5], 25
	v_readlane_b32 s12, v251, 36
	v_readlane_b32 s13, v251, 37
	s_add_u32 s4, s12, s4
	s_addc_u32 s5, s13, s5
	s_lshl_b32 s84, s83, 15
	s_and_b32 s84, s84, 0x1ff8000
	s_add_u32 s84, s4, s84
	s_addc_u32 s85, s5, 0
	s_lshl_b32 s4, s83, 12
	s_lshl_b32 s5, s82, 11
	s_sub_i32 s4, s5, s4
	s_ashr_i32 s5, s4, 31
	s_lshl_b64 s[4:5], s[4:5], 2
	s_add_u32 s4, s84, s4
	s_addc_u32 s5, s85, s5
	v_lshlrev_b32_e32 v2, 2, v208
	v_lshl_add_u64 v[238:239], s[4:5], 0, v[2:3]
	s_add_i32 m0, s41, 0x24000
	v_lshl_add_u64 v[238:239], v[238:239], 0, s[42:43]
	global_load_lds_dwordx4 v2, s[4:5] nt
	s_add_i32 m0, s41, 0x26000
	s_add_i32 s77, s77, 1
	global_load_lds_dwordx4 v[238:239], off nt
	s_branch .LBB0_167
